# baseline (speedup 1.0000x reference)
.Lmy_attn_dmadone:
	v_exp_f32_e32 v2, v2
	v_exp_f32_e32 v22, v3
	v_exp_f32_e32 v3, v4
	v_exp_f32_e32 v23, v5
	v_exp_f32_e32 v4, v6
	v_exp_f32_e32 v6, v7
	v_exp_f32_e32 v5, v8
	v_exp_f32_e32 v7, v9
	v_exp_f32_e32 v10, v10
	v_exp_f32_e32 v11, v11
	v_exp_f32_e32 v12, v12
	v_exp_f32_e32 v13, v13
	v_exp_f32_e32 v8, v14
	v_exp_f32_e32 v14, v15
	v_exp_f32_e32 v9, v16
	v_exp_f32_e32 v15, v17
	v_cvt_pk_bf16_f32 v5, v5, v7
	v_cvt_pk_bf16_f32 v4, v4, v6
	v_cvt_pk_bf16_f32 v3, v3, v23
	v_cvt_pk_bf16_f32 v2, v2, v22
	v_cvt_pk_bf16_f32 v9, v9, v15
	v_cvt_pk_bf16_f32 v8, v8, v14
	v_cvt_pk_bf16_f32 v7, v12, v13
	v_cvt_pk_bf16_f32 v6, v10, v11
	s_nop 1
	v_permlane16_swap_b32_e32 v2, v6
	v_permlane16_swap_b32_e32 v3, v7
	v_permlane16_swap_b32_e32 v4, v8
	v_permlane16_swap_b32_e32 v5, v9
	v_exp_f32_e32 v114, v24
	v_exp_f32_e32 v22, v26
	v_exp_f32_e32 v23, v28
	v_exp_f32_e32 v24, v30
	s_waitcnt lgkmcnt(0)
	v_mfma_f32_16x16x32_bf16 v[6:9], v[118:121], v[6:9], v[18:21]
	ds_read_b128 v[10:13], v89 offset:39936
	ds_read_b128 v[14:17], v89 offset:40960
	ds_read_b128 v[106:109], v89 offset:41984
	ds_read_b128 v[110:113], v89 offset:43008
	v_exp_f32_e32 v18, v31
	v_exp_f32_e32 v19, v29
	v_exp_f32_e32 v20, v27
	v_mfma_f32_16x16x32_bf16 v[2:5], v[118:121], v[2:5], v[84:87]
	s_nop 2
	v_exp_f32_e32 v84, v25
	v_cvt_pk_bf16_f32 v87, v24, v18
	v_cvt_pk_bf16_f32 v86, v23, v19
	v_cvt_pk_bf16_f32 v85, v22, v20
	s_waitcnt lgkmcnt(2)
	v_mfma_f32_32x32x16_f16 v[16:31], v[14:17], v[72:75], 0
	v_exp_f32_e32 v14, v32
	v_exp_f32_e32 v15, v34
	v_exp_f32_e32 v32, v36
	v_exp_f32_e32 v34, v37
	v_exp_f32_e32 v36, v38
	v_exp_f32_e32 v37, v39
	v_exp_f32_e32 v38, v35
	s_waitcnt lgkmcnt(1)
	v_mfma_f32_32x32x16_f16 v[16:31], v[106:109], v[76:79], v[16:31]
	v_exp_f32_e32 v39, v33
	v_cvt_pk_bf16_f32 v84, v114, v84
	v_cvt_pk_bf16_f32 v35, v36, v37
	v_cvt_pk_bf16_f32 v34, v32, v34
	v_cvt_pk_bf16_f32 v33, v15, v38
	v_cvt_pk_bf16_f32 v32, v14, v39
	s_nop 1
	v_permlane16_swap_b32_e32 v84, v32
	v_permlane16_swap_b32_e32 v85, v33
	v_permlane16_swap_b32_e32 v86, v34
	v_permlane16_swap_b32_e32 v87, v35
	ds_read_b128 v[36:39], v89 offset:44032
	s_nop 0
	v_mfma_f32_16x16x32_bf16 v[84:87], v[10:13], v[84:87], v[2:5]
	s_nop 2
	ds_read_b128 v[2:5], v89 offset:45056
	s_waitcnt lgkmcnt(2)
	v_mfma_f32_32x32x16_f16 v[16:31], v[110:113], v[80:83], v[16:31]
	v_mfma_f32_16x16x32_bf16 v[106:109], v[10:13], v[32:35], v[6:9]
	s_nop 10
	v_exp_f32_e32 v114, v16
	v_exp_f32_e32 v118, v17
	v_exp_f32_e32 v18, v18
	s_waitcnt lgkmcnt(0)
	v_mfma_f32_32x32x16_f16 v[2:17], v[2:5], v[72:75], 0
	v_exp_f32_e32 v20, v20
	v_exp_f32_e32 v21, v21
	v_exp_f32_e32 v19, v19
	ds_read_b128 v[32:35], v89 offset:46080
	ds_read_b128 v[110:113], v89 offset:47104
	v_cvt_pk_bf16_f32 v114, v114, v118
	v_cvt_pk_bf16_f32 v116, v20, v21
	v_cvt_pk_bf16_f32 v115, v18, v19
	ds_read_b128 v[118:121], v89 offset:48128
	ds_read_b128 v[18:21], v89 offset:49152
	v_exp_f32_e32 v22, v22
	v_exp_f32_e32 v23, v23
	s_waitcnt lgkmcnt(3)
	v_mfma_f32_32x32x16_f16 v[2:17], v[32:35], v[76:79], v[2:17]
	v_exp_f32_e32 v29, v29
	v_exp_f32_e32 v27, v27
	v_cvt_pk_bf16_f32 v117, v22, v23
	v_exp_f32_e32 v22, v24
	v_exp_f32_e32 v23, v26
	v_exp_f32_e32 v24, v28
	v_exp_f32_e32 v26, v30
	v_exp_f32_e32 v28, v31
	v_exp_f32_e32 v25, v25
	ds_read_b128 v[122:125], v89 offset:50176
	s_waitcnt lgkmcnt(3)
	v_mfma_f32_32x32x16_f16 v[2:17], v[110:113], v[80:83], v[2:17]
	v_cvt_pk_bf16_f32 v113, v26, v28
	v_cvt_pk_bf16_f32 v112, v24, v29
	v_cvt_pk_bf16_f32 v111, v23, v27
	v_cvt_pk_bf16_f32 v110, v22, v25
	s_nop 1
	v_permlane16_swap_b32_e32 v114, v110
	v_permlane16_swap_b32_e32 v115, v111
	s_waitcnt lgkmcnt(1)
	v_mfma_f32_32x32x16_f16 v[18:33], v[18:21], v[72:75], 0
	v_permlane16_swap_b32_e32 v116, v112
	v_permlane16_swap_b32_e32 v117, v113
	v_exp_f32_e32 v2, v2
	v_exp_f32_e32 v4, v4
	v_exp_f32_e32 v5, v5
	v_mfma_f32_16x16x32_bf16 v[84:87], v[36:39], v[114:117], v[84:87]
	v_exp_f32_e32 v3, v3
	v_exp_f32_e32 v6, v6
	v_exp_f32_e32 v7, v7
	v_mfma_f32_16x16x32_bf16 v[34:37], v[36:39], v[110:113], v[106:109]
	ds_read_b128 v[110:113], v89 offset:52224
	v_exp_f32_e32 v8, v8
	v_exp_f32_e32 v9, v9
	ds_read_b128 v[106:109], v89 offset:51200
	s_waitcnt lgkmcnt(2)
	v_mfma_f32_32x32x16_f16 v[18:33], v[122:125], v[76:79], v[18:33]
	v_exp_f32_e32 v13, v13
	v_exp_f32_e32 v11, v11
	ds_read_b128 v[122:125], v89 offset:54272
	s_waitcnt lgkmcnt(1)
	v_mfma_f32_32x32x16_f16 v[18:33], v[106:109], v[80:83], v[18:33]
	v_cvt_pk_bf16_f32 v107, v4, v5
	v_cvt_pk_bf16_f32 v106, v2, v3
	ds_read_b128 v[2:5], v89 offset:53248
	v_cvt_pk_bf16_f32 v109, v8, v9
	v_cvt_pk_bf16_f32 v108, v6, v7
	v_exp_f32_e32 v6, v10
	v_exp_f32_e32 v7, v12
	v_exp_f32_e32 v8, v14
	v_exp_f32_e32 v9, v16
	v_exp_f32_e32 v10, v17
	v_exp_f32_e32 v12, v15
	v_cvt_pk_bf16_f32 v115, v7, v13
	v_cvt_pk_bf16_f32 v114, v6, v11
	v_cvt_pk_bf16_f32 v117, v9, v10
	v_cvt_pk_bf16_f32 v116, v8, v12
	s_waitcnt lgkmcnt(0)
	v_mfma_f32_32x32x16_f16 v[2:17], v[2:5], v[72:75], 0
	v_permlane16_swap_b32_e32 v106, v114
	v_permlane16_swap_b32_e32 v107, v115
	v_permlane16_swap_b32_e32 v108, v116
	v_permlane16_swap_b32_e32 v109, v117
	v_mfma_f32_32x32x16_f16 v[2:17], v[122:125], v[76:79], v[2:17]
	v_exp_f32_e32 v18, v18
	v_exp_f32_e32 v20, v20
	v_exp_f32_e32 v21, v21
	v_exp_f32_e32 v19, v19
	v_exp_f32_e32 v22, v22
	v_exp_f32_e32 v24, v24
	v_exp_f32_e32 v25, v25
	v_mfma_f32_16x16x32_bf16 v[84:87], v[118:121], v[106:109], v[84:87]
	v_exp_f32_e32 v23, v23
	v_exp_f32_e32 v29, v29
	v_exp_f32_e32 v27, v27
	v_mfma_f32_16x16x32_bf16 v[34:37], v[118:121], v[114:117], v[34:37]
	ds_read_b128 v[106:109], v89 offset:55296
	ds_read_b128 v[114:117], v89 offset:56320
	ds_read_b128 v[122:125], v89 offset:58368
	s_waitcnt lgkmcnt(2)
	v_mfma_f32_32x32x16_f16 v[2:17], v[106:109], v[80:83], v[2:17]
	v_cvt_pk_bf16_f32 v107, v20, v21
	v_cvt_pk_bf16_f32 v106, v18, v19
	ds_read_b128 v[18:21], v89 offset:57344
	v_cvt_pk_bf16_f32 v109, v24, v25
	v_cvt_pk_bf16_f32 v108, v22, v23
	v_exp_f32_e32 v22, v26
	v_exp_f32_e32 v23, v28
	v_exp_f32_e32 v24, v30
	v_exp_f32_e32 v25, v32
	v_exp_f32_e32 v26, v33
	v_exp_f32_e32 v28, v31
	v_cvt_pk_bf16_f32 v119, v23, v29
	v_cvt_pk_bf16_f32 v118, v22, v27
	v_cvt_pk_bf16_f32 v121, v25, v26
	v_cvt_pk_bf16_f32 v120, v24, v28
	s_waitcnt lgkmcnt(0)
	v_mfma_f32_32x32x16_f16 v[18:33], v[18:21], v[72:75], 0
	v_permlane16_swap_b32_e32 v106, v118
	v_permlane16_swap_b32_e32 v107, v119
	v_permlane16_swap_b32_e32 v108, v120
	v_permlane16_swap_b32_e32 v109, v121
	v_mfma_f32_32x32x16_f16 v[18:33], v[122:125], v[76:79], v[18:33]
	v_exp_f32_e32 v2, v2
	v_exp_f32_e32 v4, v4
	v_exp_f32_e32 v5, v5
	v_exp_f32_e32 v3, v3
	v_exp_f32_e32 v6, v6
	v_exp_f32_e32 v8, v8
	v_exp_f32_e32 v9, v9
	v_mfma_f32_16x16x32_bf16 v[84:87], v[110:113], v[106:109], v[84:87]
	v_exp_f32_e32 v7, v7
	v_exp_f32_e32 v13, v13
	v_exp_f32_e32 v11, v11
	v_mfma_f32_16x16x32_bf16 v[34:37], v[110:113], v[118:121], v[34:37]
	ds_read_b128 v[106:109], v89 offset:59392
	ds_read_b128 v[110:113], v89 offset:60416
	ds_read_b128 v[122:125], v89 offset:62464
	s_waitcnt lgkmcnt(2)
	v_mfma_f32_32x32x16_f16 v[18:33], v[106:109], v[80:83], v[18:33]
	v_cvt_pk_bf16_f32 v107, v4, v5
	v_cvt_pk_bf16_f32 v106, v2, v3
	ds_read_b128 v[2:5], v89 offset:61440
	v_cvt_pk_bf16_f32 v109, v8, v9
	v_cvt_pk_bf16_f32 v108, v6, v7
	v_exp_f32_e32 v6, v10
	v_exp_f32_e32 v7, v12
	v_exp_f32_e32 v8, v14
	v_exp_f32_e32 v9, v16
	v_exp_f32_e32 v10, v17
	v_exp_f32_e32 v12, v15
	v_cvt_pk_bf16_f32 v119, v7, v13
	v_cvt_pk_bf16_f32 v118, v6, v11
	v_cvt_pk_bf16_f32 v121, v9, v10
	v_cvt_pk_bf16_f32 v120, v8, v12
	s_waitcnt lgkmcnt(0)
	v_mfma_f32_32x32x16_f16 v[2:17], v[2:5], v[72:75], 0
	v_permlane16_swap_b32_e32 v106, v118
	v_permlane16_swap_b32_e32 v107, v119
	v_permlane16_swap_b32_e32 v108, v120
	v_permlane16_swap_b32_e32 v109, v121
	v_mfma_f32_32x32x16_f16 v[2:17], v[122:125], v[76:79], v[2:17]
	v_exp_f32_e32 v38, v20
	v_exp_f32_e32 v20, v22
	v_exp_f32_e32 v22, v24
	v_exp_f32_e32 v24, v25
	v_exp_f32_e32 v25, v21
	v_exp_f32_e32 v23, v23
	v_exp_f32_e32 v39, v19
	v_mfma_f32_16x16x32_bf16 v[84:87], v[114:117], v[106:109], v[84:87]
	v_cvt_pk_bf16_f32 v21, v22, v24
	v_cvt_pk_bf16_f32 v19, v38, v25
	v_exp_f32_e32 v22, v26
	v_mfma_f32_16x16x32_bf16 v[34:37], v[114:117], v[118:121], v[34:37]
	ds_read_b128 v[106:109], v89 offset:63488
	ds_read_b128 v[114:117], v89 offset:64512
	v_exp_f32_e32 v25, v32
	v_exp_f32_e32 v26, v33
	s_waitcnt lgkmcnt(1)
	v_mfma_f32_32x32x16_f16 v[2:17], v[106:109], v[80:83], v[2:17]
	v_exp_f32_e32 v18, v18
	v_cvt_pk_bf16_f32 v20, v20, v23
	v_exp_f32_e32 v23, v28
	v_exp_f32_e32 v24, v30
	v_exp_f32_e32 v28, v31
	v_exp_f32_e32 v29, v29
	v_exp_f32_e32 v27, v27
	v_cvt_pk_bf16_f32 v25, v25, v26
	s_nop 3
	v_exp_f32_e32 v26, v4
	v_exp_f32_e32 v4, v6
	v_exp_f32_e32 v6, v8
	v_exp_f32_e32 v8, v9
	v_exp_f32_e32 v7, v7
	v_exp_f32_e32 v9, v5
	v_cvt_pk_bf16_f32 v18, v18, v39
	v_cvt_pk_bf16_f32 v24, v24, v28
	v_cvt_pk_bf16_f32 v23, v23, v29
	v_cvt_pk_bf16_f32 v22, v22, v27
	v_exp_f32_e32 v2, v2
	v_exp_f32_e32 v27, v3
	v_cvt_pk_bf16_f32 v5, v6, v8
	v_cvt_pk_bf16_f32 v4, v4, v7
	v_cvt_pk_bf16_f32 v3, v26, v9
	v_exp_f32_e32 v6, v10
	v_exp_f32_e32 v7, v12
	v_exp_f32_e32 v8, v14
	v_exp_f32_e32 v9, v16
	v_exp_f32_e32 v10, v17
	v_exp_f32_e32 v12, v15
	v_exp_f32_e32 v13, v13
	v_exp_f32_e32 v11, v11
	v_permlane16_swap_b32_e32 v18, v22
	v_permlane16_swap_b32_e32 v19, v23
	v_permlane16_swap_b32_e32 v20, v24
	v_permlane16_swap_b32_e32 v21, v25
	v_cvt_pk_bf16_f32 v2, v2, v27
	s_nop 0
	v_mfma_f32_16x16x32_bf16 v[18:21], v[110:113], v[18:21], v[84:87]
	v_cvt_pk_bf16_f32 v9, v9, v10
	v_cvt_pk_bf16_f32 v8, v8, v12
	v_cvt_pk_bf16_f32 v7, v7, v13
	v_mfma_f32_16x16x32_bf16 v[22:25], v[110:113], v[22:25], v[34:37]
	v_cvt_pk_bf16_f32 v6, v6, v11
	s_nop 1
	v_permlane16_swap_b32_e32 v2, v6
	v_permlane16_swap_b32_e32 v3, v7
	v_permlane16_swap_b32_e32 v4, v8
	v_permlane16_swap_b32_e32 v5, v9
	s_waitcnt lgkmcnt(0)
	s_nop 0
	v_mfma_f32_16x16x32_bf16 v[84:87], v[114:117], v[2:5], v[18:21]
	s_waitcnt vmcnt(0)
	s_barrier
	s_cmp_lt_u32 s48, 0x1000
	s_cbranch_scc1 .Lmy_dph_1
	s_sleep 1
.Lmy_dph_1:
	v_mfma_f32_16x16x32_bf16 v[18:21], v[114:117], v[6:9], v[22:25]
	s_cbranch_vccnz .LBB3_13

.LBB3_9:
	ds_read_b128 v[2:5], v89
	ds_read_b128 v[22:25], v89 offset:1024
	s_xor_b64 s[6:7], s[6:7], -1
	s_andn2_b64 vcc, exec, s[6:7]
	s_waitcnt lgkmcnt(1)
	v_mfma_f32_32x32x16_f16 v[2:17], v[2:5], v[72:75], 0
	s_waitcnt lgkmcnt(0)
	v_mfma_f32_32x32x16_f16 v[2:17], v[22:25], v[76:79], v[2:17]
	ds_read_b128 v[22:25], v89 offset:4096
	ds_read_b128 v[106:109], v89 offset:5120
	ds_read_b128 v[110:113], v89 offset:2048
	ds_read_b128 v[114:117], v89 offset:6144
	ds_read_b128 v[118:121], v89 offset:3072
	s_waitcnt lgkmcnt(4)
	v_mfma_f32_32x32x16_f16 v[24:39], v[22:25], v[72:75], 0
	s_waitcnt lgkmcnt(3)
	v_mfma_f32_32x32x16_f16 v[24:39], v[106:109], v[76:79], v[24:39]
	s_waitcnt lgkmcnt(2)
	v_mfma_f32_32x32x16_f16 v[2:17], v[110:113], v[80:83], v[2:17]
	s_waitcnt lgkmcnt(1)
	v_mfma_f32_32x32x16_f16 v[24:39], v[114:117], v[80:83], v[24:39]
	s_add_u32 m0, s48, 0x8000
	s_nop 0
	global_load_lds_dwordx4 v88, s[50:51]
	s_add_u32 s54, s50, 0x2000
	s_addc_u32 s55, s51, 0
	s_add_u32 m0, s48, 0xa000
	s_nop 0
	global_load_lds_dwordx4 v88, s[54:55]
	s_add_u32 s54, s50, 0x4000
	s_addc_u32 s55, s51, 0
	s_add_u32 m0, s48, 0xc000
	s_nop 0
	global_load_lds_dwordx4 v88, s[54:55]
	s_add_u32 s54, s50, 0x6000
	s_addc_u32 s55, s51, 0
	s_add_u32 m0, s48, 0xe000
	s_nop 0
	global_load_lds_dwordx4 v88, s[54:55]
	s_add_u32 s50, s50, 0x10000
	s_addc_u32 s51, s51, 0
	v_exp_f32_e32 v2, v2
	v_exp_f32_e32 v22, v3
	v_exp_f32_e32 v3, v4
	v_exp_f32_e32 v23, v5
	v_exp_f32_e32 v4, v6
	v_exp_f32_e32 v6, v7
	v_exp_f32_e32 v5, v8
	v_exp_f32_e32 v7, v9
	v_exp_f32_e32 v10, v10
	v_exp_f32_e32 v11, v11
	v_exp_f32_e32 v12, v12
	v_exp_f32_e32 v13, v13
	v_exp_f32_e32 v8, v14
	v_exp_f32_e32 v14, v15
	v_exp_f32_e32 v9, v16
	v_exp_f32_e32 v15, v17
	v_cvt_pk_bf16_f32 v5, v5, v7
	v_cvt_pk_bf16_f32 v4, v4, v6
	v_cvt_pk_bf16_f32 v3, v3, v23
	v_cvt_pk_bf16_f32 v2, v2, v22
	v_cvt_pk_bf16_f32 v9, v9, v15
	v_cvt_pk_bf16_f32 v8, v8, v14
	v_cvt_pk_bf16_f32 v7, v12, v13
	v_cvt_pk_bf16_f32 v6, v10, v11
	s_nop 1
	v_permlane16_swap_b32_e32 v2, v6
	v_permlane16_swap_b32_e32 v3, v7
	v_permlane16_swap_b32_e32 v4, v8
	v_permlane16_swap_b32_e32 v5, v9
	v_exp_f32_e32 v114, v24
	v_exp_f32_e32 v22, v26
	v_exp_f32_e32 v23, v28
	v_exp_f32_e32 v24, v30
	s_waitcnt lgkmcnt(0)
	v_mfma_f32_16x16x32_bf16 v[6:9], v[118:121], v[6:9], v[18:21]
	ds_read_b128 v[10:13], v89 offset:7168
	ds_read_b128 v[14:17], v89 offset:8192
	ds_read_b128 v[106:109], v89 offset:9216
	ds_read_b128 v[110:113], v89 offset:10240
	v_exp_f32_e32 v18, v31
	v_exp_f32_e32 v19, v29
	v_exp_f32_e32 v20, v27
	v_mfma_f32_16x16x32_bf16 v[2:5], v[118:121], v[2:5], v[84:87]
	s_nop 2
	v_exp_f32_e32 v84, v25
	v_cvt_pk_bf16_f32 v87, v24, v18
	v_cvt_pk_bf16_f32 v86, v23, v19
	v_cvt_pk_bf16_f32 v85, v22, v20
	s_waitcnt lgkmcnt(2)
	v_mfma_f32_32x32x16_f16 v[16:31], v[14:17], v[72:75], 0
	v_exp_f32_e32 v14, v32
	v_exp_f32_e32 v15, v34
	v_exp_f32_e32 v32, v36
	v_exp_f32_e32 v34, v37
	v_exp_f32_e32 v36, v38
	v_exp_f32_e32 v37, v39
	v_exp_f32_e32 v38, v35
	s_waitcnt lgkmcnt(1)
	v_mfma_f32_32x32x16_f16 v[16:31], v[106:109], v[76:79], v[16:31]
	v_exp_f32_e32 v39, v33
	v_cvt_pk_bf16_f32 v84, v114, v84
	v_cvt_pk_bf16_f32 v35, v36, v37
	v_cvt_pk_bf16_f32 v34, v32, v34
	v_cvt_pk_bf16_f32 v33, v15, v38
	v_cvt_pk_bf16_f32 v32, v14, v39
	s_nop 1
	v_permlane16_swap_b32_e32 v84, v32
	v_permlane16_swap_b32_e32 v85, v33
	v_permlane16_swap_b32_e32 v86, v34
	v_permlane16_swap_b32_e32 v87, v35
	ds_read_b128 v[36:39], v89 offset:11264
	s_nop 0
	v_mfma_f32_16x16x32_bf16 v[84:87], v[10:13], v[84:87], v[2:5]
	s_nop 2
	ds_read_b128 v[2:5], v89 offset:12288
	s_waitcnt lgkmcnt(2)
	v_mfma_f32_32x32x16_f16 v[16:31], v[110:113], v[80:83], v[16:31]
	v_mfma_f32_16x16x32_bf16 v[106:109], v[10:13], v[32:35], v[6:9]
	s_nop 10
	v_exp_f32_e32 v114, v16
	v_exp_f32_e32 v118, v17
	v_exp_f32_e32 v18, v18
	s_waitcnt lgkmcnt(0)
	v_mfma_f32_32x32x16_f16 v[2:17], v[2:5], v[72:75], 0
	v_exp_f32_e32 v20, v20
	v_exp_f32_e32 v21, v21
	v_exp_f32_e32 v19, v19
	ds_read_b128 v[32:35], v89 offset:13312
	ds_read_b128 v[110:113], v89 offset:14336
	v_cvt_pk_bf16_f32 v114, v114, v118
	v_cvt_pk_bf16_f32 v116, v20, v21
	v_cvt_pk_bf16_f32 v115, v18, v19
	ds_read_b128 v[118:121], v89 offset:15360
	ds_read_b128 v[18:21], v89 offset:16384
	v_exp_f32_e32 v22, v22
	v_exp_f32_e32 v23, v23
	s_waitcnt lgkmcnt(3)
	v_mfma_f32_32x32x16_f16 v[2:17], v[32:35], v[76:79], v[2:17]
	v_exp_f32_e32 v29, v29
	v_exp_f32_e32 v27, v27
	v_cvt_pk_bf16_f32 v117, v22, v23
	v_exp_f32_e32 v22, v24
	v_exp_f32_e32 v23, v26
	v_exp_f32_e32 v24, v28
	v_exp_f32_e32 v26, v30
	v_exp_f32_e32 v28, v31
	v_exp_f32_e32 v25, v25
	ds_read_b128 v[122:125], v89 offset:17408
	s_waitcnt lgkmcnt(3)
	v_mfma_f32_32x32x16_f16 v[2:17], v[110:113], v[80:83], v[2:17]
	v_cvt_pk_bf16_f32 v113, v26, v28
	v_cvt_pk_bf16_f32 v112, v24, v29
	v_cvt_pk_bf16_f32 v111, v23, v27
	v_cvt_pk_bf16_f32 v110, v22, v25
	s_nop 1
	v_permlane16_swap_b32_e32 v114, v110
	v_permlane16_swap_b32_e32 v115, v111
	s_waitcnt lgkmcnt(1)
	v_mfma_f32_32x32x16_f16 v[18:33], v[18:21], v[72:75], 0
	v_permlane16_swap_b32_e32 v116, v112
	v_permlane16_swap_b32_e32 v117, v113
	v_exp_f32_e32 v2, v2
	v_exp_f32_e32 v4, v4
	v_exp_f32_e32 v5, v5
	v_mfma_f32_16x16x32_bf16 v[84:87], v[36:39], v[114:117], v[84:87]
	v_exp_f32_e32 v3, v3
	v_exp_f32_e32 v6, v6
	v_exp_f32_e32 v7, v7
	v_mfma_f32_16x16x32_bf16 v[34:37], v[36:39], v[110:113], v[106:109]
	ds_read_b128 v[110:113], v89 offset:19456
	v_exp_f32_e32 v8, v8
	v_exp_f32_e32 v9, v9
	ds_read_b128 v[106:109], v89 offset:18432
	s_waitcnt lgkmcnt(2)
	v_mfma_f32_32x32x16_f16 v[18:33], v[122:125], v[76:79], v[18:33]
	v_exp_f32_e32 v13, v13
	v_exp_f32_e32 v11, v11
	ds_read_b128 v[122:125], v89 offset:21504
	s_waitcnt lgkmcnt(1)
	v_mfma_f32_32x32x16_f16 v[18:33], v[106:109], v[80:83], v[18:33]
	v_cvt_pk_bf16_f32 v107, v4, v5
	v_cvt_pk_bf16_f32 v106, v2, v3
	ds_read_b128 v[2:5], v89 offset:20480
	v_cvt_pk_bf16_f32 v109, v8, v9
	v_cvt_pk_bf16_f32 v108, v6, v7
	v_exp_f32_e32 v6, v10
	v_exp_f32_e32 v7, v12
	v_exp_f32_e32 v8, v14
	v_exp_f32_e32 v9, v16
	v_exp_f32_e32 v10, v17
	v_exp_f32_e32 v12, v15
	v_cvt_pk_bf16_f32 v115, v7, v13
	v_cvt_pk_bf16_f32 v114, v6, v11
	v_cvt_pk_bf16_f32 v117, v9, v10
	v_cvt_pk_bf16_f32 v116, v8, v12
	s_waitcnt lgkmcnt(0)
	v_mfma_f32_32x32x16_f16 v[2:17], v[2:5], v[72:75], 0
	v_permlane16_swap_b32_e32 v106, v114
	v_permlane16_swap_b32_e32 v107, v115
	v_permlane16_swap_b32_e32 v108, v116
	v_permlane16_swap_b32_e32 v109, v117
	v_mfma_f32_32x32x16_f16 v[2:17], v[122:125], v[76:79], v[2:17]
	v_exp_f32_e32 v18, v18
	v_exp_f32_e32 v20, v20
	v_exp_f32_e32 v21, v21
	v_exp_f32_e32 v19, v19
	v_exp_f32_e32 v22, v22
	v_exp_f32_e32 v24, v24
	v_exp_f32_e32 v25, v25
	v_mfma_f32_16x16x32_bf16 v[84:87], v[118:121], v[106:109], v[84:87]
	v_exp_f32_e32 v23, v23
	v_exp_f32_e32 v29, v29
	v_exp_f32_e32 v27, v27
	v_mfma_f32_16x16x32_bf16 v[34:37], v[118:121], v[114:117], v[34:37]
	ds_read_b128 v[106:109], v89 offset:22528
	ds_read_b128 v[114:117], v89 offset:23552
	ds_read_b128 v[122:125], v89 offset:25600
	s_waitcnt lgkmcnt(2)
	v_mfma_f32_32x32x16_f16 v[2:17], v[106:109], v[80:83], v[2:17]
	v_cvt_pk_bf16_f32 v107, v20, v21
	v_cvt_pk_bf16_f32 v106, v18, v19
	ds_read_b128 v[18:21], v89 offset:24576
	v_cvt_pk_bf16_f32 v109, v24, v25
	v_cvt_pk_bf16_f32 v108, v22, v23
	v_exp_f32_e32 v22, v26
	v_exp_f32_e32 v23, v28
	v_exp_f32_e32 v24, v30
	v_exp_f32_e32 v25, v32
	v_exp_f32_e32 v26, v33
	v_exp_f32_e32 v28, v31
	v_cvt_pk_bf16_f32 v119, v23, v29
	v_cvt_pk_bf16_f32 v118, v22, v27
	v_cvt_pk_bf16_f32 v121, v25, v26
	v_cvt_pk_bf16_f32 v120, v24, v28
	s_waitcnt lgkmcnt(0)
	v_mfma_f32_32x32x16_f16 v[18:33], v[18:21], v[72:75], 0
	v_permlane16_swap_b32_e32 v106, v118
	v_permlane16_swap_b32_e32 v107, v119
	v_permlane16_swap_b32_e32 v108, v120
	v_permlane16_swap_b32_e32 v109, v121
	v_mfma_f32_32x32x16_f16 v[18:33], v[122:125], v[76:79], v[18:33]
	v_exp_f32_e32 v2, v2
	v_exp_f32_e32 v4, v4
	v_exp_f32_e32 v5, v5
	v_exp_f32_e32 v3, v3
	v_exp_f32_e32 v6, v6
	v_exp_f32_e32 v8, v8
	v_exp_f32_e32 v9, v9
	v_mfma_f32_16x16x32_bf16 v[84:87], v[110:113], v[106:109], v[84:87]
	v_exp_f32_e32 v7, v7
	v_exp_f32_e32 v13, v13
	v_exp_f32_e32 v11, v11
	v_mfma_f32_16x16x32_bf16 v[34:37], v[110:113], v[118:121], v[34:37]
	ds_read_b128 v[106:109], v89 offset:26624
	ds_read_b128 v[110:113], v89 offset:27648
	ds_read_b128 v[122:125], v89 offset:29696
	s_waitcnt lgkmcnt(2)
	v_mfma_f32_32x32x16_f16 v[18:33], v[106:109], v[80:83], v[18:33]
	v_cvt_pk_bf16_f32 v107, v4, v5
	v_cvt_pk_bf16_f32 v106, v2, v3
	ds_read_b128 v[2:5], v89 offset:28672
	v_cvt_pk_bf16_f32 v109, v8, v9
	v_cvt_pk_bf16_f32 v108, v6, v7
	v_exp_f32_e32 v6, v10
	v_exp_f32_e32 v7, v12
	v_exp_f32_e32 v8, v14
	v_exp_f32_e32 v9, v16
	v_exp_f32_e32 v10, v17
	v_exp_f32_e32 v12, v15
	v_cvt_pk_bf16_f32 v119, v7, v13
	v_cvt_pk_bf16_f32 v118, v6, v11
	v_cvt_pk_bf16_f32 v121, v9, v10
	v_cvt_pk_bf16_f32 v120, v8, v12
	s_waitcnt lgkmcnt(0)
	v_mfma_f32_32x32x16_f16 v[2:17], v[2:5], v[72:75], 0
	v_permlane16_swap_b32_e32 v106, v118
	v_permlane16_swap_b32_e32 v107, v119
	v_permlane16_swap_b32_e32 v108, v120
	v_permlane16_swap_b32_e32 v109, v121
	v_mfma_f32_32x32x16_f16 v[2:17], v[122:125], v[76:79], v[2:17]
	v_exp_f32_e32 v38, v20
	v_exp_f32_e32 v20, v22
	v_exp_f32_e32 v22, v24
	v_exp_f32_e32 v24, v25
	v_exp_f32_e32 v25, v21
	v_exp_f32_e32 v23, v23
	v_exp_f32_e32 v39, v19
	v_mfma_f32_16x16x32_bf16 v[84:87], v[114:117], v[106:109], v[84:87]
	v_cvt_pk_bf16_f32 v21, v22, v24
	v_cvt_pk_bf16_f32 v19, v38, v25
	v_exp_f32_e32 v22, v26
	v_mfma_f32_16x16x32_bf16 v[34:37], v[114:117], v[118:121], v[34:37]
	ds_read_b128 v[106:109], v89 offset:30720
	ds_read_b128 v[114:117], v89 offset:31744
	v_exp_f32_e32 v25, v32
	v_exp_f32_e32 v26, v33
	s_waitcnt lgkmcnt(1)
	v_mfma_f32_32x32x16_f16 v[2:17], v[106:109], v[80:83], v[2:17]
	v_exp_f32_e32 v18, v18
	v_cvt_pk_bf16_f32 v20, v20, v23
	v_exp_f32_e32 v23, v28
	v_exp_f32_e32 v24, v30
	v_exp_f32_e32 v28, v31
	v_exp_f32_e32 v29, v29
	v_exp_f32_e32 v27, v27
	v_cvt_pk_bf16_f32 v25, v25, v26
	s_nop 3
	v_exp_f32_e32 v26, v4
	v_exp_f32_e32 v4, v6
	v_exp_f32_e32 v6, v8
	v_exp_f32_e32 v8, v9
	v_exp_f32_e32 v7, v7
	v_exp_f32_e32 v9, v5
	v_cvt_pk_bf16_f32 v18, v18, v39
	v_cvt_pk_bf16_f32 v24, v24, v28
	v_cvt_pk_bf16_f32 v23, v23, v29
	v_cvt_pk_bf16_f32 v22, v22, v27
	v_exp_f32_e32 v2, v2
	v_exp_f32_e32 v27, v3
	v_cvt_pk_bf16_f32 v5, v6, v8
	v_cvt_pk_bf16_f32 v4, v4, v7
	v_cvt_pk_bf16_f32 v3, v26, v9
	v_exp_f32_e32 v6, v10
	v_exp_f32_e32 v7, v12
	v_exp_f32_e32 v8, v14
	v_exp_f32_e32 v9, v16
	v_exp_f32_e32 v10, v17
	v_exp_f32_e32 v12, v15
	v_exp_f32_e32 v13, v13
	v_exp_f32_e32 v11, v11
	v_permlane16_swap_b32_e32 v18, v22
	v_permlane16_swap_b32_e32 v19, v23
	v_permlane16_swap_b32_e32 v20, v24
	v_permlane16_swap_b32_e32 v21, v25
	v_cvt_pk_bf16_f32 v2, v2, v27
	s_nop 0
	v_mfma_f32_16x16x32_bf16 v[18:21], v[110:113], v[18:21], v[84:87]
	v_cvt_pk_bf16_f32 v9, v9, v10
	v_cvt_pk_bf16_f32 v8, v8, v12
	v_cvt_pk_bf16_f32 v7, v7, v13
	v_mfma_f32_16x16x32_bf16 v[22:25], v[110:113], v[22:25], v[34:37]
	v_cvt_pk_bf16_f32 v6, v6, v11
	s_nop 1
	v_permlane16_swap_b32_e32 v2, v6
	v_permlane16_swap_b32_e32 v3, v7
	v_permlane16_swap_b32_e32 v4, v8
	v_permlane16_swap_b32_e32 v5, v9
	s_waitcnt lgkmcnt(0)
	s_nop 0
	v_mfma_f32_16x16x32_bf16 v[84:87], v[114:117], v[2:5], v[18:21]
	s_waitcnt vmcnt(0)
	s_barrier
	s_cmp_lt_u32 s48, 0x1000
	s_cbranch_scc1 .Lmy_dph_0
	s_sleep 1
.Lmy_dph_0:
	v_mfma_f32_16x16x32_bf16 v[18:21], v[114:117], v[6:9], v[22:25]
	s_branch .LBB3_6
